# router weight staging into LDS: 8 batches of 8 loads in flight with counted waits instead of 64 serialized load/wait iterations; plus previous changes
# speedup vs baseline: 1.0035x; 1.0035x over previous
; __device__ __forceinline__ float bf2f(bf16_t b) { return __uint_as_float(((unsigned)b) << 16); }
; __device__ __forceinline__ bf16_t f2bf(float f) { return (bf16_t)(cvt_pk_bf16(f, 0.f) & 0xffffu); }
; __device__ __forceinline__ void phase_norm2_route(const Frame& F, const Params& P, int l, int nrows, long long dctx) {
;     ...
;     for (int i = F.tid; i < DM * NEXP; i += NTHR) {
;         const int d = i >> 5, e = i & 31; const float w = wr[i]; const bf16_t h = f2bf(w);
;         whi[e * WROW + d] = h; wlo[e * WROW + d] = f2bf(w - bf2f(h));
;     }
.LBB0_916:
	v_readlane_b32 s18, v252, 4
	v_readlane_b32 s19, v252, 5
	s_cmp_gt_i32 s18, s0
	s_cselect_b64 s[8:9], -1, 0
	s_cmp_ge_i32 s0, s19
	s_cselect_b64 s[0:1], -1, 0
	s_or_b64 s[0:1], s[8:9], s[0:1]
	s_and_b64 vcc, exec, s[0:1]
	s_cbranch_vccnz .LBB0_1716
	s_waitcnt vmcnt(0)
	v_mov_b32_e32 v30, v0
	s_mov_b32 s1, 0x8000
	s_nop 0
	v_readfirstlane_b32 s0, v30
	v_cmp_gt_i32_e32 vcc, s1, v30
	s_and_saveexec_b64 s[8:9], vcc
	s_cbranch_execz .LBB0_920
	v_readlane_b32 s18, v255, 9
	v_readlane_b32 s19, v255, 10
	v_readlane_b32 s28, v254, 56
	s_lshl_b64 s[18:19], s[18:19], 17
	v_readlane_b32 s30, v254, 58
	v_readlane_b32 s31, v254, 59
	s_add_u32 s18, s30, s18
	v_and_b32_e32 v1, 31, v30
	v_ashrrev_i32_e32 v31, 31, v30
	s_addc_u32 s19, s31, s19
	v_mul_u32_u24_e32 v1, 0x408, v1
	v_lshl_add_u64 v[2:3], v[30:31], 2, s[18:19]
	s_mov_b64 s[18:19], 0
	v_mov_b32_e32 v4, v30
	v_readlane_b32 s29, v254, 57
	v_ashrrev_i32_e32 v6, 5, v4
	v_add_u32_e32 v6, v6, v1
	v_lshl_add_u32 v6, v6, 1, 0
	v_add_u32_e32 v7, 0x10200, v6
	s_mov_b32 s1, 8
.Lrt_loop:
	global_load_dword v10, v[2:3], off
	v_lshl_add_u64 v[2:3], v[2:3], 0, s[38:39]
	global_load_dword v11, v[2:3], off
	v_lshl_add_u64 v[2:3], v[2:3], 0, s[38:39]
	global_load_dword v12, v[2:3], off
	v_lshl_add_u64 v[2:3], v[2:3], 0, s[38:39]
	global_load_dword v13, v[2:3], off
	v_lshl_add_u64 v[2:3], v[2:3], 0, s[38:39]
	global_load_dword v14, v[2:3], off
	v_lshl_add_u64 v[2:3], v[2:3], 0, s[38:39]
	global_load_dword v15, v[2:3], off
	v_lshl_add_u64 v[2:3], v[2:3], 0, s[38:39]
	global_load_dword v16, v[2:3], off
	v_lshl_add_u64 v[2:3], v[2:3], 0, s[38:39]
	global_load_dword v17, v[2:3], off
	v_lshl_add_u64 v[2:3], v[2:3], 0, s[38:39]
	s_waitcnt vmcnt(7)
	v_cvt_pk_bf16_f32 v8, v10, v147
	ds_write_b16 v6, v8
	v_lshlrev_b32_e32 v9, 16, v8
	v_sub_f32_e32 v10, v10, v9
	v_cvt_pk_bf16_f32 v10, v10, v147
	ds_write_b16 v7, v10
	s_waitcnt vmcnt(6)
	v_cvt_pk_bf16_f32 v8, v11, v147
	ds_write_b16 v6, v8 offset:32
	v_lshlrev_b32_e32 v9, 16, v8
	v_sub_f32_e32 v11, v11, v9
	v_cvt_pk_bf16_f32 v11, v11, v147
	ds_write_b16 v7, v11 offset:32
	s_waitcnt vmcnt(5)
	v_cvt_pk_bf16_f32 v8, v12, v147
	ds_write_b16 v6, v8 offset:64
	v_lshlrev_b32_e32 v9, 16, v8
	v_sub_f32_e32 v12, v12, v9
	v_cvt_pk_bf16_f32 v12, v12, v147
	ds_write_b16 v7, v12 offset:64
	s_waitcnt vmcnt(4)
	v_cvt_pk_bf16_f32 v8, v13, v147
	ds_write_b16 v6, v8 offset:96
	v_lshlrev_b32_e32 v9, 16, v8
	v_sub_f32_e32 v13, v13, v9
	v_cvt_pk_bf16_f32 v13, v13, v147
	ds_write_b16 v7, v13 offset:96
	s_waitcnt vmcnt(3)
	v_cvt_pk_bf16_f32 v8, v14, v147
	ds_write_b16 v6, v8 offset:128
	v_lshlrev_b32_e32 v9, 16, v8
	v_sub_f32_e32 v14, v14, v9
	v_cvt_pk_bf16_f32 v14, v14, v147
	ds_write_b16 v7, v14 offset:128
	s_waitcnt vmcnt(2)
	v_cvt_pk_bf16_f32 v8, v15, v147
	ds_write_b16 v6, v8 offset:160
	v_lshlrev_b32_e32 v9, 16, v8
	v_sub_f32_e32 v15, v15, v9
	v_cvt_pk_bf16_f32 v15, v15, v147
	ds_write_b16 v7, v15 offset:160
	s_waitcnt vmcnt(1)
	v_cvt_pk_bf16_f32 v8, v16, v147
	ds_write_b16 v6, v8 offset:192
	v_lshlrev_b32_e32 v9, 16, v8
	v_sub_f32_e32 v16, v16, v9
	v_cvt_pk_bf16_f32 v16, v16, v147
	ds_write_b16 v7, v16 offset:192
	s_waitcnt vmcnt(0)
	v_cvt_pk_bf16_f32 v8, v17, v147
	ds_write_b16 v6, v8 offset:224
	v_lshlrev_b32_e32 v9, 16, v8
	v_sub_f32_e32 v17, v17, v9
	v_cvt_pk_bf16_f32 v17, v17, v147
	ds_write_b16 v7, v17 offset:224
	v_add_u32_e32 v6, 0x100, v6
	v_add_u32_e32 v7, 0x100, v7
	s_sub_u32 s1, s1, 1
	s_cmp_lg_u32 s1, 0
	s_cbranch_scc1 .Lrt_loop
